# v47 plus non-temporal stores for the layer output (out) in the combine/LN2 phase
# speedup vs baseline: 1.0260x; 1.0260x over previous
; __device__ __forceinline__ void p9_row(const KA& a, int l, int row, const LAS int* pref, int lane, int ts_l, float w_l) {
;     ...
;     int slot_l = (lane < 8) ? pref[ts_l >> 16] * 256 + (ts_l & 0xffff) : pref[64] * 256 + row;
;     if (lane >= 8) w_l = 1.f;
;     w_l *= (1.f / YS_SCALE);
;     const __amdgpu_buffer_rsrc_t yrs = __builtin_amdgcn_make_buffer_rsrc((void*)YS, 0, (unsigned)((size_t)SLOT_MAX * DM), 0x00020000);
;     const int voff = 4 * lane;
;     int yv[8][8], ys[8];
; #pragma unroll
;     for (int k = 0; k < 8; ++k) { const int soff = __builtin_amdgcn_readlane(slot_l, k) * DM;
; #pragma unroll
;         for (int j = 0; j < 8; ++j) yv[k][j] = __builtin_amdgcn_raw_buffer_load_b32(yrs, voff + 256 * j, soff, 2); }
; #pragma unroll
;     for (int k = 0; k < 8; ++k) { const float w = __builtin_bit_cast(float, __builtin_amdgcn_readlane(__builtin_bit_cast(int, w_l), k));
;         if (k == 0) { const int soff = __builtin_amdgcn_readlane(slot_l, 8) * DM;
; #pragma unroll
;             for (int j = 0; j < 8; ++j) ys[j] = __builtin_amdgcn_raw_buffer_load_b32(yrs, voff + 256 * j, soff, 2); }
; #pragma unroll
;         for (int j = 0; j < 8; ++j) { const f32x2 lo = __builtin_amdgcn_cvt_pk_f32_fp8(yv[k][j], false), hi = __builtin_amdgcn_cvt_pk_f32_fp8(yv[k][j], true);
;             m[j].x = fmaf(w, lo.x, m[j].x); m[j].y = fmaf(w, lo.y, m[j].y); m[j].z = fmaf(w, hi.x, m[j].z); m[j].w = fmaf(w, hi.y, m[j].w); } }
.LBB0_1660:
	s_or_b64 exec, exec, s[26:27]
	s_ashr_i32 s41, s0, 12
	s_add_i32 s0, s41, s37
	s_mul_hi_i32 s1, s0, 0xc000
	s_mul_i32 s0, s0, 0xc000
	s_add_u32 s0, s31, s0
	v_readlane_b32 s26, v1, 0
	s_addc_u32 s1, s35, s1
	s_lshl_b32 s27, s26, 11
	v_readlane_b32 s26, v1, 1
	s_lshl_b32 s28, s26, 11
	v_readlane_b32 s26, v1, 2
	s_lshl_b32 s30, s26, 11
	v_readlane_b32 s26, v1, 3
	s_lshl_b32 s33, s26, 11
	v_readlane_b32 s26, v1, 4
	s_lshl_b32 s34, s26, 11
	v_readlane_b32 s26, v1, 5
	s_lshl_b32 s36, s26, 11
	v_readlane_b32 s26, v1, 6
	s_lshl_b32 s38, s26, 11
	buffer_load_dword v2, v237, s[84:87], s30 offen nt
	buffer_load_dword v3, v237, s[84:87], s33 offen nt
	buffer_load_dword v4, v237, s[84:87], s34 offen nt
	buffer_load_dword v5, v237, s[84:87], s36 offen nt
	buffer_load_dword v6, v237, s[84:87], s38 offen nt
	buffer_load_dword v7, v234, s[84:87], s27 offen nt
	buffer_load_dword v10, v234, s[84:87], s28 offen nt
	buffer_load_dword v11, v234, s[84:87], s30 offen nt
	buffer_load_dword v12, v234, s[84:87], s33 offen nt
	buffer_load_dword v13, v234, s[84:87], s34 offen nt
	buffer_load_dword v8, v237, s[84:87], s28 offen nt
	buffer_load_dword v9, v237, s[84:87], s27 offen nt
	buffer_load_dword v14, v236, s[84:87], s33 offen nt
	buffer_load_dword v15, v236, s[84:87], s34 offen nt
	buffer_load_dword v16, v236, s[84:87], s36 offen nt
	buffer_load_dword v17, v236, s[84:87], s38 offen nt
	buffer_load_dword v18, v235, s[84:87], s27 offen nt
	buffer_load_dword v19, v235, s[84:87], s28 offen nt
	buffer_load_dword v20, v235, s[84:87], s30 offen nt
	buffer_load_dword v21, v235, s[84:87], s33 offen nt
	buffer_load_dword v22, v234, s[84:87], s36 offen nt
	buffer_load_dword v23, v234, s[84:87], s38 offen nt
	buffer_load_dword v86, v236, s[84:87], s27 offen nt
	buffer_load_dword v82, v236, s[84:87], s30 offen nt
	buffer_load_dword v84, v236, s[84:87], s28 offen nt
	buffer_load_dword v102, v235, s[84:87], s34 offen nt
	buffer_load_dword v98, v235, s[84:87], s36 offen nt
	buffer_load_dword v94, v235, s[84:87], s38 offen nt
	v_readlane_b32 s26, v1, 7
	v_readlane_b32 s42, v1, 8
	s_lshl_b32 s40, s26, 11
	buffer_load_dword v222, v33, s[84:87], s27 offen nt
	buffer_load_dword v227, v33, s[84:87], s28 offen nt
	buffer_load_dword v225, v33, s[84:87], s30 offen nt
	buffer_load_dword v229, v33, s[84:87], s33 offen nt
	buffer_load_dword v226, v33, s[84:87], s34 offen nt
	buffer_load_dword v253, v33, s[84:87], s36 offen nt
	buffer_load_dword v223, v33, s[84:87], s38 offen nt
	buffer_load_dword v246, v33, s[84:87], s40 offen nt
	s_lshl_b32 s42, s42, 11
	buffer_load_dword v202, v32, s[84:87], s28 offen nt
	buffer_load_dword v200, v32, s[84:87], s30 offen nt
	buffer_load_dword v208, v32, s[84:87], s33 offen nt
	buffer_load_dword v210, v32, s[84:87], s34 offen nt
	buffer_load_dword v211, v32, s[84:87], s36 offen nt
	buffer_load_dword v212, v32, s[84:87], s38 offen nt
	buffer_load_dword v214, v32, s[84:87], s40 offen nt
	buffer_load_dword v215, v32, s[84:87], s42 offen nt
	buffer_load_dword v216, v232, s[84:87], s27 offen nt
	buffer_load_dword v213, v232, s[84:87], s28 offen nt
	buffer_load_dword v217, v232, s[84:87], s30 offen nt
	buffer_load_dword v194, v232, s[84:87], s33 offen nt
	buffer_load_dword v186, v232, s[84:87], s34 offen nt
	buffer_load_dword v182, v232, s[84:87], s36 offen nt
	buffer_load_dword v178, v232, s[84:87], s38 offen nt
	buffer_load_dword v252, v33, s[84:87], s42 offen nt
	buffer_load_dword v174, v233, s[84:87], s27 offen nt
	buffer_load_dword v172, v233, s[84:87], s28 offen nt
	buffer_load_dword v170, v233, s[84:87], s30 offen nt
	buffer_load_dword v166, v233, s[84:87], s33 offen nt
	buffer_load_dword v162, v233, s[84:87], s34 offen nt
	buffer_load_dword v158, v233, s[84:87], s36 offen nt
	buffer_load_dword v251, v232, s[84:87], s40 offen nt
	buffer_load_dword v244, v232, s[84:87], s42 offen nt
	buffer_load_dword v154, v233, s[84:87], s38 offen nt
	buffer_load_dword v250, v233, s[84:87], s40 offen nt
	buffer_load_dword v243, v233, s[84:87], s42 offen nt
	buffer_load_dword v249, v234, s[84:87], s40 offen nt
	buffer_load_dword v242, v234, s[84:87], s42 offen nt
	buffer_load_dword v248, v235, s[84:87], s40 offen nt
	buffer_load_dword v241, v235, s[84:87], s42 offen nt
	buffer_load_dword v247, v236, s[84:87], s40 offen nt
	buffer_load_dword v240, v236, s[84:87], s42 offen nt
	buffer_load_dword v203, v32, s[84:87], s27 offen nt
	buffer_load_dword v245, v237, s[84:87], s40 offen nt
	buffer_load_dword v239, v237, s[84:87], s42 offen nt
	v_lshlrev_b32_e32 v192, 2, v32
	s_waitcnt vmcnt(62)
	v_mul_f32_e32 v0, 0x3d800000, v0
	v_mov_b32_e32 v24, 0x3d800000
	v_cndmask_b32_e64 v0, v0, v24, s[6:7]
	s_mov_b32 s44, 0x3d800000
	v_readlane_b32 s26, v0, 0
	v_readlane_b32 s42, v0, 1
	v_readlane_b32 s40, v0, 2
	v_readlane_b32 s38, v0, 3
	v_readlane_b32 s36, v0, 4
	v_readlane_b32 s34, v0, 5
	v_readlane_b32 s30, v0, 6
	v_readlane_b32 s28, v0, 7
	v_cvt_pk_f32_fp8_sdwa v[44:45], v2 src0_sel:WORD_1
	v_cvt_pk_f32_fp8_sdwa v[40:41], v3 src0_sel:WORD_1
	v_cvt_pk_f32_fp8_e32 v[50:51], v3
	v_cvt_pk_f32_fp8_e32 v[54:55], v2
	v_cvt_pk_f32_fp8_sdwa v[24:25], v6 src0_sel:WORD_1
	v_cvt_pk_f32_fp8_sdwa v[26:27], v5 src0_sel:WORD_1
	v_cvt_pk_f32_fp8_sdwa v[134:135], v10 src0_sel:WORD_1
	v_cvt_pk_f32_fp8_sdwa v[130:131], v11 src0_sel:WORD_1
	v_cvt_pk_f32_fp8_e32 v[140:141], v11
	v_cvt_pk_f32_fp8_e32 v[142:143], v10
	s_waitcnt vmcnt(61)
	v_cvt_pk_f32_fp8_sdwa v[48:49], v8 src0_sel:WORD_1
	s_waitcnt vmcnt(60)
; __device__ __forceinline__ void p9_row(const KA& a, int l, int row, const LAS int* pref, int lane, int ts_l, float w_l) {
;     ...
;     for (int k = 0; k < 8; ++k) { const int soff = __builtin_amdgcn_readlane(slot_l, k) * DM;
; #pragma unroll
;         for (int j = 0; j < 8; ++j) yv[k][j] = __builtin_amdgcn_raw_buffer_load_b32(yrs, voff + 256 * j, soff, 2); }
; #pragma unroll
;     for (int k = 0; k < 8; ++k) { const float w = __builtin_bit_cast(float, __builtin_amdgcn_readlane(__builtin_bit_cast(int, w_l), k));
;         if (k == 0) { const int soff = __builtin_amdgcn_readlane(slot_l, 8) * DM;
; #pragma unroll
;             for (int j = 0; j < 8; ++j) ys[j] = __builtin_amdgcn_raw_buffer_load_b32(yrs, voff + 256 * j, soff, 2); }
; #pragma unroll
;         for (int j = 0; j < 8; ++j) { const f32x2 lo = __builtin_amdgcn_cvt_pk_f32_fp8(yv[k][j], false), hi = __builtin_amdgcn_cvt_pk_f32_fp8(yv[k][j], true);
;             m[j].x = fmaf(w, lo.x, m[j].x); m[j].y = fmaf(w, lo.y, m[j].y); m[j].z = fmaf(w, hi.x, m[j].z); m[j].w = fmaf(w, hi.y, m[j].w); } }
;     { const float w = 1.f / YS_SCALE;
; #pragma unroll
;         for (int j = 0; j < 8; ++j) { const f32x2 lo = __builtin_amdgcn_cvt_pk_f32_fp8(ys[j], false), hi = __builtin_amdgcn_cvt_pk_f32_fp8(ys[j], true);
;             m[j].x = fmaf(w, lo.x, m[j].x); m[j].y = fmaf(w, lo.y, m[j].y); m[j].z = fmaf(w, hi.x, m[j].z); m[j].w = fmaf(w, hi.y, m[j].w); } }
;     asm volatile("" ::: "memory");
;     f32x4 v[8];
; #pragma unroll
;     for (int j = 0; j < 8; ++j) { const f32x4 x1 = __builtin_nontemporal_load((const f32x4*)(X1 + (size_t)row * DM + 4 * lane + 256 * j)), g = *(const f32x4*)(gf + 4 * lane + 256 * j) + 1.0f;
;         v[j] = x1 * DN_ALPHA + g * m[j]; }
	v_cvt_pk_f32_fp8_sdwa v[52:53], v9 src0_sel:WORD_1
	v_cvt_pk_f32_fp8_e32 v[56:57], v8
	v_cvt_pk_f32_fp8_e32 v[58:59], v9
	v_lshl_add_u64 v[8:9], s[0:1], 0, v[192:193]
	s_mov_b32 s0, 0xb000
	v_add_co_u32_e32 v116, vcc, s0, v8
	v_lshl_add_u64 v[10:11], s[10:11], 0, v[38:39]
	s_nop 0
	v_addc_co_u32_e32 v117, vcc, 0, v9, vcc
	s_mov_b32 s0, 0x11001000
	global_load_dwordx4 v[0:3], v[116:117], off offset:-4096
	v_add_co_u32_e32 v148, vcc, s0, v10
	v_cvt_pk_f32_fp8_sdwa v[28:29], v4 src0_sel:WORD_1
	s_nop 0
	v_addc_co_u32_e32 v149, vcc, 0, v11, vcc
	v_cvt_pk_f32_fp8_e32 v[30:31], v6
	v_cvt_pk_f32_fp8_e32 v[42:43], v5
	v_cvt_pk_f32_fp8_e32 v[46:47], v4
	v_cvt_pk_f32_fp8_sdwa v[138:139], v7 src0_sel:WORD_1
	v_cvt_pk_f32_fp8_e32 v[144:145], v7
	global_load_dwordx4 v[4:7], v[148:149], off offset:-4096 nt
	s_mov_b64 s[0:1], 0xa000
	v_lshl_add_u64 v[218:219], v[8:9], 0, s[0:1]
	s_waitcnt vmcnt(58)
	v_cvt_pk_f32_fp8_sdwa v[60:61], v17 src0_sel:WORD_1
	v_cvt_pk_f32_fp8_sdwa v[62:63], v16 src0_sel:WORD_1
	v_cvt_pk_f32_fp8_e32 v[72:73], v17
	v_cvt_pk_f32_fp8_e32 v[74:75], v16
	s_waitcnt vmcnt(56)
	v_cvt_pk_f32_fp8_sdwa v[104:105], v19 src0_sel:WORD_1
	v_cvt_pk_f32_fp8_sdwa v[108:109], v18 src0_sel:WORD_1
	v_cvt_pk_f32_fp8_e32 v[112:113], v19
	v_cvt_pk_f32_fp8_e32 v[114:115], v18
	global_load_dwordx4 v[16:19], v[218:219], off offset:1024
	s_mov_b32 s0, 0x11000000
	v_add_co_u32_e32 v204, vcc, s0, v10
	v_cvt_pk_f32_fp8_sdwa v[64:65], v15 src0_sel:WORD_1
	v_cvt_pk_f32_fp8_sdwa v[66:67], v14 src0_sel:WORD_1
	v_cvt_pk_f32_fp8_e32 v[76:77], v15
	v_cvt_pk_f32_fp8_e32 v[78:79], v14
	s_waitcnt vmcnt(5)
	v_cvt_pk_f32_fp8_sdwa v[14:15], v203 src0_sel:WORD_1
	v_addc_co_u32_e32 v205, vcc, 0, v11, vcc
	v_cvt_pk_f32_fp8_e32 v[10:11], v203
	v_cvt_pk_f32_fp8_sdwa v[122:123], v13 src0_sel:WORD_1
	v_cvt_pk_f32_fp8_sdwa v[126:127], v12 src0_sel:WORD_1
	v_cvt_pk_f32_fp8_e32 v[132:133], v13
	v_cvt_pk_f32_fp8_e32 v[136:137], v12
	v_cvt_pk_f32_fp8_sdwa v[12:13], v202 src0_sel:WORD_1
	v_cvt_pk_f32_fp8_e32 v[202:203], v202
	v_cvt_pk_f32_fp8_sdwa v[96:97], v21 src0_sel:WORD_1
	v_cvt_pk_f32_fp8_sdwa v[100:101], v20 src0_sel:WORD_1
	v_cvt_pk_f32_fp8_e32 v[106:107], v21
	v_cvt_pk_f32_fp8_e32 v[110:111], v20
	v_cvt_pk_f32_fp8_sdwa v[20:21], v200 src0_sel:WORD_1
	v_cvt_pk_f32_fp8_e32 v[200:201], v200
	v_cvt_pk_f32_fp8_sdwa v[8:9], v208 src0_sel:WORD_1
	v_pk_fma_f32 v[14:15], s[26:27], v[14:15], 0 op_sel_hi:[0,1,0]
	v_pk_fma_f32 v[10:11], s[26:27], v[10:11], 0 op_sel_hi:[0,1,0]
	v_pk_fma_f32 v[206:207], s[42:43], v[12:13], v[14:15] op_sel_hi:[0,1,1]
	v_pk_fma_f32 v[10:11], s[42:43], v[202:203], v[10:11] op_sel_hi:[0,1,1]
	v_pk_fma_f32 v[202:203], s[40:41], v[200:201], v[10:11] op_sel_hi:[0,1,1]
	v_pk_fma_f32 v[10:11], s[40:41], v[20:21], v[206:207] op_sel_hi:[0,1,1]
	v_pk_fma_f32 v[20:21], s[38:39], v[8:9], v[10:11] op_sel_hi:[0,1,1]
	global_load_dwordx4 v[8:11], v[218:219], off offset:2048
	global_load_dwordx4 v[12:15], v[204:205], off offset:1024 nt
	v_cvt_pk_f32_fp8_e32 v[208:209], v208
	v_cvt_pk_f32_fp8_sdwa v[206:207], v210 src0_sel:WORD_1
	v_cvt_pk_f32_fp8_sdwa v[118:119], v23 src0_sel:WORD_1
	v_cvt_pk_f32_fp8_sdwa v[120:121], v22 src0_sel:WORD_1
	v_pk_fma_f32 v[202:203], s[38:39], v[208:209], v[202:203] op_sel_hi:[0,1,1]
	v_cvt_pk_f32_fp8_sdwa v[208:209], v211 src0_sel:WORD_1
	v_cvt_pk_f32_fp8_e32 v[124:125], v23
	v_cvt_pk_f32_fp8_e32 v[128:129], v22
	v_cvt_pk_f32_fp8_e32 v[22:23], v210
	v_pk_fma_f32 v[20:21], s[36:37], v[206:207], v[20:21] op_sel_hi:[0,1,1]
	v_cvt_pk_f32_fp8_e32 v[206:207], v211
	v_pk_fma_f32 v[20:21], s[34:35], v[208:209], v[20:21] op_sel_hi:[0,1,1]
	v_cvt_pk_f32_fp8_e32 v[208:209], v212
	v_cvt_pk_f32_fp8_sdwa v[210:211], v212 src0_sel:WORD_1
	v_pk_fma_f32 v[22:23], s[36:37], v[22:23], v[202:203] op_sel_hi:[0,1,1]
	v_pk_fma_f32 v[22:23], s[34:35], v[206:207], v[22:23] op_sel_hi:[0,1,1]
	v_pk_fma_f32 v[22:23], s[30:31], v[208:209], v[22:23] op_sel_hi:[0,1,1]
	v_cvt_pk_f32_fp8_e32 v[208:209], v214
	v_cvt_pk_f32_fp8_sdwa v[196:197], v213 src0_sel:WORD_1
	v_cvt_pk_f32_fp8_e32 v[202:203], v213
	v_cvt_pk_f32_fp8_sdwa v[212:213], v214 src0_sel:WORD_1
	v_pk_fma_f32 v[20:21], s[30:31], v[210:211], v[20:21] op_sel_hi:[0,1,1]
	v_cvt_pk_f32_fp8_e32 v[210:211], v215
	v_cvt_pk_f32_fp8_sdwa v[214:215], v215 src0_sel:WORD_1
	v_pk_fma_f32 v[22:23], s[28:29], v[208:209], v[22:23] op_sel_hi:[0,1,1]
	s_waitcnt vmcnt(4)
	v_pk_add_f32 v[0:1], v[0:1], 1.0 op_sel_hi:[1,0]
	v_pk_fma_f32 v[20:21], s[28:29], v[212:213], v[20:21] op_sel_hi:[0,1,1]
	v_pk_fma_f32 v[22:23], v[210:211], s[44:45], v[22:23] op_sel_hi:[1,0,1]
	v_pk_add_f32 v[2:3], v[2:3], 1.0 op_sel_hi:[1,0]
	v_pk_fma_f32 v[20:21], v[214:215], s[44:45], v[20:21] op_sel_hi:[1,0,1]
	v_pk_mul_f32 v[0:1], v[22:23], v[0:1]
	s_mov_b32 s0, 0x3fb504f3
	v_pk_mul_f32 v[2:3], v[20:21], v[2:3]
	v_cvt_pk_f32_fp8_sdwa v[230:231], v222 src0_sel:WORD_1
	v_cvt_pk_f32_fp8_sdwa v[220:221], v227 src0_sel:WORD_1
	s_waitcnt vmcnt(3)
	v_pk_fma_f32 v[22:23], v[4:5], s[0:1], v[0:1] op_sel_hi:[1,0,1]
	v_cvt_pk_f32_fp8_e32 v[0:1], v222
	v_pk_fma_f32 v[20:21], v[6:7], s[0:1], v[2:3] op_sel_hi:[1,0,1]
	v_cvt_pk_f32_fp8_e32 v[2:3], v227
	v_cvt_pk_f32_fp8_sdwa v[190:191], v217 src0_sel:WORD_1
	v_cvt_pk_f32_fp8_sdwa v[198:199], v216 src0_sel:WORD_1
	v_cvt_pk_f32_fp8_e32 v[200:201], v217
	v_cvt_pk_f32_fp8_e32 v[206:207], v216
	v_cvt_pk_f32_fp8_sdwa v[216:217], v225 src0_sel:WORD_1
	v_cvt_pk_f32_fp8_sdwa v[212:213], v229 src0_sel:WORD_1
	v_cvt_pk_f32_fp8_e32 v[214:215], v229
	s_waitcnt vmcnt(2)
; __device__ __forceinline__ void p9_row(const KA& a, int l, int row, const LAS int* pref, int lane, int ts_l, float w_l) {
;     ...
;     for (int k = 0; k < 8; ++k) { const float w = __builtin_bit_cast(float, __builtin_amdgcn_readlane(__builtin_bit_cast(int, w_l), k));
;         if (k == 0) { const int soff = __builtin_amdgcn_readlane(slot_l, 8) * DM;
; #pragma unroll
;             for (int j = 0; j < 8; ++j) ys[j] = __builtin_amdgcn_raw_buffer_load_b32(yrs, voff + 256 * j, soff, 2); }
; #pragma unroll
;         for (int j = 0; j < 8; ++j) { const f32x2 lo = __builtin_amdgcn_cvt_pk_f32_fp8(yv[k][j], false), hi = __builtin_amdgcn_cvt_pk_f32_fp8(yv[k][j], true);
;             m[j].x = fmaf(w, lo.x, m[j].x); m[j].y = fmaf(w, lo.y, m[j].y); m[j].z = fmaf(w, hi.x, m[j].z); m[j].w = fmaf(w, hi.y, m[j].w); } }
;     { const float w = 1.f / YS_SCALE;
; #pragma unroll
;         for (int j = 0; j < 8; ++j) { const f32x2 lo = __builtin_amdgcn_cvt_pk_f32_fp8(ys[j], false), hi = __builtin_amdgcn_cvt_pk_f32_fp8(ys[j], true);
;             m[j].x = fmaf(w, lo.x, m[j].x); m[j].y = fmaf(w, lo.y, m[j].y); m[j].z = fmaf(w, hi.x, m[j].z); m[j].w = fmaf(w, hi.y, m[j].w); } }
;     asm volatile("" ::: "memory");
;     f32x4 v[8];
; #pragma unroll
;     for (int j = 0; j < 8; ++j) { const f32x4 x1 = __builtin_nontemporal_load((const f32x4*)(X1 + (size_t)row * DM + 4 * lane + 256 * j)), g = *(const f32x4*)(gf + 4 * lane + 256 * j) + 1.0f;
;         v[j] = x1 * DN_ALPHA + g * m[j]; }
	v_pk_add_f32 v[210:211], v[16:17], 1.0 op_sel_hi:[1,0]
	v_cvt_pk_f32_fp8_e32 v[16:17], v225
	v_pk_fma_f32 v[4:5], s[26:27], v[230:231], 0 op_sel_hi:[0,1,0]
	v_pk_fma_f32 v[0:1], s[26:27], v[0:1], 0 op_sel_hi:[0,1,0]
	v_pk_add_f32 v[208:209], v[18:19], 1.0 op_sel_hi:[1,0]
	v_pk_fma_f32 v[18:19], s[42:43], v[2:3], v[0:1] op_sel_hi:[0,1,1]
	v_pk_fma_f32 v[0:1], s[42:43], v[220:221], v[4:5] op_sel_hi:[0,1,1]
	v_pk_fma_f32 v[216:217], s[40:41], v[216:217], v[0:1] op_sel_hi:[0,1,1]
	global_load_dwordx4 v[0:3], v[218:219], off offset:3072
	v_pk_fma_f32 v[218:219], s[40:41], v[16:17], v[18:19] op_sel_hi:[0,1,1]
	v_pk_fma_f32 v[214:215], s[38:39], v[214:215], v[218:219] op_sel_hi:[0,1,1]
	v_cvt_pk_f32_fp8_sdwa v[218:219], v226 src0_sel:WORD_1
	v_pk_fma_f32 v[212:213], s[38:39], v[212:213], v[216:217] op_sel_hi:[0,1,1]
	v_cvt_pk_f32_fp8_e32 v[216:217], v226
	v_cvt_pk_f32_fp8_sdwa v[220:221], v223 src0_sel:WORD_1
	v_pk_fma_f32 v[212:213], s[36:37], v[218:219], v[212:213] op_sel_hi:[0,1,1]
	v_cvt_pk_f32_fp8_e32 v[218:219], v253
	v_pk_fma_f32 v[214:215], s[36:37], v[216:217], v[214:215] op_sel_hi:[0,1,1]
	v_cvt_pk_f32_fp8_sdwa v[216:217], v253 src0_sel:WORD_1
	v_cvt_pk_f32_fp8_e32 v[222:223], v223
	v_cvt_pk_f32_fp8_e32 v[230:231], v246
	v_pk_fma_f32 v[218:219], s[34:35], v[218:219], v[214:215] op_sel_hi:[0,1,1]
	v_pk_fma_f32 v[212:213], s[34:35], v[216:217], v[212:213] op_sel_hi:[0,1,1]
	v_pk_fma_f32 v[216:217], s[30:31], v[220:221], v[212:213] op_sel_hi:[0,1,1]
	v_pk_fma_f32 v[218:219], s[30:31], v[222:223], v[218:219] op_sel_hi:[0,1,1]
	v_cvt_pk_f32_fp8_sdwa v[220:221], v246 src0_sel:WORD_1
	v_pk_fma_f32 v[222:223], s[28:29], v[230:231], v[218:219] op_sel_hi:[0,1,1]
	v_cvt_pk_f32_fp8_sdwa v[218:219], v252 src0_sel:WORD_1
	v_cvt_pk_f32_fp8_e32 v[230:231], v252
	v_cvt_pk_f32_fp8_sdwa v[188:189], v194 src0_sel:WORD_1
	v_cvt_pk_f32_fp8_e32 v[194:195], v194
	v_pk_fma_f32 v[216:217], s[28:29], v[220:221], v[216:217] op_sel_hi:[0,1,1]
	v_cvt_pk_f32_fp8_sdwa v[184:185], v186 src0_sel:WORD_1
	v_cvt_pk_f32_fp8_e32 v[186:187], v186
	global_load_dwordx4 v[4:7], v[204:205], off offset:2048 nt
	global_load_dwordx4 v[16:19], v[148:149], off offset:3072 nt
	v_pk_fma_f32 v[226:227], v[218:219], s[44:45], v[216:217] op_sel_hi:[1,0,1]
	global_load_dwordx4 v[216:219], v[204:205], off offset:3072 nt
	v_pk_fma_f32 v[204:205], v[230:231], s[44:45], v[222:223] op_sel_hi:[1,0,1]
	s_waitcnt vmcnt(5)
	v_pk_add_f32 v[230:231], v[8:9], 1.0 op_sel_hi:[1,0]
	v_pk_fma_f32 v[8:9], s[26:27], v[206:207], 0 op_sel_hi:[0,1,0]
	v_cvt_pk_f32_fp8_sdwa v[168:169], v174 src0_sel:WORD_1
	v_cvt_pk_f32_fp8_e32 v[174:175], v174
	v_cvt_pk_f32_fp8_sdwa v[180:181], v182 src0_sel:WORD_1
	v_cvt_pk_f32_fp8_e32 v[182:183], v182
	v_pk_mul_f32 v[208:209], v[226:227], v[208:209]
	v_pk_add_f32 v[226:227], v[10:11], 1.0 op_sel_hi:[1,0]
	v_pk_fma_f32 v[8:9], s[42:43], v[202:203], v[8:9] op_sel_hi:[0,1,1]
	v_pk_fma_f32 v[10:11], s[26:27], v[198:199], 0 op_sel_hi:[0,1,0]
	v_cvt_pk_f32_fp8_sdwa v[164:165], v172 src0_sel:WORD_1
	v_cvt_pk_f32_fp8_e32 v[172:173], v172
	v_pk_fma_f32 v[10:11], s[42:43], v[196:197], v[10:11] op_sel_hi:[0,1,1]
	v_pk_fma_f32 v[8:9], s[40:41], v[200:201], v[8:9] op_sel_hi:[0,1,1]
	v_cvt_pk_f32_fp8_sdwa v[160:161], v170 src0_sel:WORD_1
	v_cvt_pk_f32_fp8_e32 v[170:171], v170
	v_cvt_pk_f32_fp8_sdwa v[176:177], v178 src0_sel:WORD_1
	v_cvt_pk_f32_fp8_e32 v[178:179], v178
	v_pk_fma_f32 v[10:11], s[40:41], v[190:191], v[10:11] op_sel_hi:[0,1,1]
	v_pk_fma_f32 v[194:195], s[38:39], v[194:195], v[8:9] op_sel_hi:[0,1,1]
	v_cvt_pk_f32_fp8_sdwa v[156:157], v166 src0_sel:WORD_1
	v_cvt_pk_f32_fp8_e32 v[166:167], v166
	v_cvt_pk_f32_fp8_e32 v[252:253], v251
	v_pk_mul_f32 v[204:205], v[204:205], v[210:211]
	v_cvt_pk_f32_fp8_sdwa v[210:211], v251 src0_sel:WORD_1
	v_pk_fma_f32 v[188:189], s[38:39], v[188:189], v[10:11] op_sel_hi:[0,1,1]
	v_pk_fma_f32 v[186:187], s[36:37], v[186:187], v[194:195] op_sel_hi:[0,1,1]
	v_cvt_pk_f32_fp8_sdwa v[152:153], v162 src0_sel:WORD_1
	v_cvt_pk_f32_fp8_e32 v[162:163], v162
	v_pk_fma_f32 v[184:185], s[36:37], v[184:185], v[188:189] op_sel_hi:[0,1,1]
	v_cvt_pk_f32_fp8_e32 v[194:195], v244
	v_pk_fma_f32 v[182:183], s[34:35], v[182:183], v[186:187] op_sel_hi:[0,1,1]
	v_cvt_pk_f32_fp8_sdwa v[186:187], v244 src0_sel:WORD_1
	v_pk_fma_f32 v[168:169], s[26:27], v[168:169], 0 op_sel_hi:[0,1,0]
	v_pk_fma_f32 v[174:175], s[26:27], v[174:175], 0 op_sel_hi:[0,1,0]
	v_cvt_pk_f32_fp8_sdwa v[150:151], v158 src0_sel:WORD_1
	v_cvt_pk_f32_fp8_e32 v[158:159], v158
	v_pk_fma_f32 v[180:181], s[34:35], v[180:181], v[184:185] op_sel_hi:[0,1,1]
	v_pk_fma_f32 v[172:173], s[42:43], v[172:173], v[174:175] op_sel_hi:[0,1,1]
	v_pk_fma_f32 v[164:165], s[42:43], v[164:165], v[168:169] op_sel_hi:[0,1,1]
	v_cvt_pk_f32_fp8_sdwa v[146:147], v154 src0_sel:WORD_1
	v_cvt_pk_f32_fp8_e32 v[154:155], v154
	v_pk_fma_f32 v[176:177], s[30:31], v[176:177], v[180:181] op_sel_hi:[0,1,1]
	v_pk_fma_f32 v[178:179], s[30:31], v[178:179], v[182:183] op_sel_hi:[0,1,1]
	v_pk_fma_f32 v[160:161], s[40:41], v[160:161], v[164:165] op_sel_hi:[0,1,1]
	v_pk_fma_f32 v[164:165], s[40:41], v[170:171], v[172:173] op_sel_hi:[0,1,1]
	s_waitcnt vmcnt(4)
; __device__ __forceinline__ void p9_row(const KA& a, int l, int row, const LAS int* pref, int lane, int ts_l, float w_l) {
;     ...
;     for (int k = 0; k < 8; ++k) { const float w = __builtin_bit_cast(float, __builtin_amdgcn_readlane(__builtin_bit_cast(int, w_l), k));
;         if (k == 0) { const int soff = __builtin_amdgcn_readlane(slot_l, 8) * DM;
; #pragma unroll
;             for (int j = 0; j < 8; ++j) ys[j] = __builtin_amdgcn_raw_buffer_load_b32(yrs, voff + 256 * j, soff, 2); }
; #pragma unroll
;         for (int j = 0; j < 8; ++j) { const f32x2 lo = __builtin_amdgcn_cvt_pk_f32_fp8(yv[k][j], false), hi = __builtin_amdgcn_cvt_pk_f32_fp8(yv[k][j], true);
;             m[j].x = fmaf(w, lo.x, m[j].x); m[j].y = fmaf(w, lo.y, m[j].y); m[j].z = fmaf(w, hi.x, m[j].z); m[j].w = fmaf(w, hi.y, m[j].w); } }
;     { const float w = 1.f / YS_SCALE;
; #pragma unroll
;         for (int j = 0; j < 8; ++j) { const f32x2 lo = __builtin_amdgcn_cvt_pk_f32_fp8(ys[j], false), hi = __builtin_amdgcn_cvt_pk_f32_fp8(ys[j], true);
;             m[j].x = fmaf(w, lo.x, m[j].x); m[j].y = fmaf(w, lo.y, m[j].y); m[j].z = fmaf(w, hi.x, m[j].z); m[j].w = fmaf(w, hi.y, m[j].w); } }
;     asm volatile("" ::: "memory");
;     f32x4 v[8];
; #pragma unroll
;     for (int j = 0; j < 8; ++j) { const f32x4 x1 = __builtin_nontemporal_load((const f32x4*)(X1 + (size_t)row * DM + 4 * lane + 256 * j)), g = *(const f32x4*)(gf + 4 * lane + 256 * j) + 1.0f;
;         v[j] = x1 * DN_ALPHA + g * m[j]; }
	v_pk_fma_f32 v[12:13], v[12:13], s[0:1], v[204:205] op_sel_hi:[1,0,1]
	v_cvt_pk_f32_fp8_e32 v[204:205], v250
	v_pk_fma_f32 v[178:179], s[28:29], v[252:253], v[178:179] op_sel_hi:[0,1,1]
	v_pk_fma_f32 v[176:177], s[28:29], v[210:211], v[176:177] op_sel_hi:[0,1,1]
	v_pk_fma_f32 v[164:165], s[38:39], v[166:167], v[164:165] op_sel_hi:[0,1,1]
	v_pk_fma_f32 v[156:157], s[38:39], v[156:157], v[160:161] op_sel_hi:[0,1,1]
	global_load_dwordx4 v[220:223], v[116:117], off
	global_load_dwordx4 v[8:11], v[116:117], off offset:1024
	v_pk_fma_f32 v[180:181], v[186:187], s[44:45], v[176:177] op_sel_hi:[1,0,1]
	v_pk_fma_f32 v[182:183], v[194:195], s[44:45], v[178:179] op_sel_hi:[1,0,1]
	v_pk_fma_f32 v[152:153], s[36:37], v[152:153], v[156:157] op_sel_hi:[0,1,1]
	v_pk_fma_f32 v[156:157], s[36:37], v[162:163], v[164:165] op_sel_hi:[0,1,1]
	v_pk_mul_f32 v[186:187], v[182:183], v[230:231]
	v_pk_mul_f32 v[194:195], v[180:181], v[226:227]
	global_load_dwordx4 v[180:183], v[116:117], off offset:2048
	v_pk_fma_f32 v[156:157], s[34:35], v[158:159], v[156:157] op_sel_hi:[0,1,1]
	v_pk_fma_f32 v[150:151], s[34:35], v[150:151], v[152:153] op_sel_hi:[0,1,1]
	v_pk_fma_f32 v[152:153], s[30:31], v[154:155], v[156:157] op_sel_hi:[0,1,1]
	global_load_dwordx4 v[212:215], v[148:149], off nt
	global_load_dwordx4 v[176:179], v[148:149], off offset:1024 nt
	v_pk_fma_f32 v[146:147], s[30:31], v[146:147], v[150:151] op_sel_hi:[0,1,1]
	global_load_dwordx4 v[148:151], v[148:149], off offset:2048 nt
	v_pk_fma_f32 v[156:157], s[28:29], v[204:205], v[152:153] op_sel_hi:[0,1,1]
	global_load_dwordx4 v[152:155], v[116:117], off offset:3072
	v_cvt_pk_f32_fp8_sdwa v[80:81], v86 src0_sel:WORD_1
	v_cvt_pk_f32_fp8_e32 v[86:87], v86
	v_cvt_pk_f32_fp8_sdwa v[70:71], v84 src0_sel:WORD_1
	v_cvt_pk_f32_fp8_e32 v[84:85], v84
	v_cvt_pk_f32_fp8_sdwa v[68:69], v82 src0_sel:WORD_1
	v_cvt_pk_f32_fp8_e32 v[82:83], v82
	v_cvt_pk_f32_fp8_sdwa v[92:93], v102 src0_sel:WORD_1
	v_cvt_pk_f32_fp8_e32 v[102:103], v102
	v_pk_fma_f32 v[114:115], s[26:27], v[114:115], 0 op_sel_hi:[0,1,0]
	v_pk_fma_f32 v[108:109], s[26:27], v[108:109], 0 op_sel_hi:[0,1,0]
	v_cvt_pk_f32_fp8_sdwa v[90:91], v98 src0_sel:WORD_1
	v_cvt_pk_f32_fp8_e32 v[98:99], v98
	v_pk_fma_f32 v[104:105], s[42:43], v[104:105], v[108:109] op_sel_hi:[0,1,1]
	v_pk_fma_f32 v[108:109], s[42:43], v[112:113], v[114:115] op_sel_hi:[0,1,1]
	v_pk_fma_f32 v[86:87], s[26:27], v[86:87], 0 op_sel_hi:[0,1,0]
	v_pk_fma_f32 v[80:81], s[26:27], v[80:81], 0 op_sel_hi:[0,1,0]
	v_cvt_pk_f32_fp8_sdwa v[88:89], v94 src0_sel:WORD_1
	v_cvt_pk_f32_fp8_e32 v[94:95], v94
	v_pk_fma_f32 v[108:109], s[40:41], v[110:111], v[108:109] op_sel_hi:[0,1,1]
	v_pk_fma_f32 v[100:101], s[40:41], v[100:101], v[104:105] op_sel_hi:[0,1,1]
	v_pk_fma_f32 v[70:71], s[42:43], v[70:71], v[80:81] op_sel_hi:[0,1,1]
	v_pk_fma_f32 v[80:81], s[42:43], v[84:85], v[86:87] op_sel_hi:[0,1,1]
	v_cvt_pk_f32_fp8_e32 v[196:197], v248
	v_cvt_pk_f32_fp8_sdwa v[198:199], v248 src0_sel:WORD_1
	v_pk_fma_f32 v[96:97], s[38:39], v[96:97], v[100:101] op_sel_hi:[0,1,1]
	v_pk_fma_f32 v[100:101], s[38:39], v[106:107], v[108:109] op_sel_hi:[0,1,1]
	v_pk_fma_f32 v[80:81], s[40:41], v[82:83], v[80:81] op_sel_hi:[0,1,1]
	v_pk_fma_f32 v[68:69], s[40:41], v[68:69], v[70:71] op_sel_hi:[0,1,1]
	v_pk_fma_f32 v[58:59], s[26:27], v[58:59], 0 op_sel_hi:[0,1,0]
	v_pk_fma_f32 v[52:53], s[26:27], v[52:53], 0 op_sel_hi:[0,1,0]
	v_pk_fma_f32 v[14:15], v[14:15], s[0:1], v[208:209] op_sel_hi:[1,0,1]
	v_cvt_pk_f32_fp8_sdwa v[208:209], v250 src0_sel:WORD_1
	v_cvt_pk_f32_fp8_e32 v[250:251], v249
	v_cvt_pk_f32_fp8_sdwa v[202:203], v249 src0_sel:WORD_1
	v_cvt_pk_f32_fp8_e32 v[190:191], v247
	v_cvt_pk_f32_fp8_sdwa v[200:201], v247 src0_sel:WORD_1
	v_cvt_pk_f32_fp8_e32 v[248:249], v241
	v_cvt_pk_f32_fp8_sdwa v[252:253], v241 src0_sel:WORD_1
	v_pk_fma_f32 v[100:101], s[36:37], v[102:103], v[100:101] op_sel_hi:[0,1,1]
	v_pk_fma_f32 v[92:93], s[36:37], v[92:93], v[96:97] op_sel_hi:[0,1,1]
	v_pk_fma_f32 v[66:67], s[38:39], v[66:67], v[68:69] op_sel_hi:[0,1,1]
	v_pk_fma_f32 v[68:69], s[38:39], v[78:79], v[80:81] op_sel_hi:[0,1,1]
	v_pk_fma_f32 v[48:49], s[42:43], v[48:49], v[52:53] op_sel_hi:[0,1,1]
	v_pk_fma_f32 v[52:53], s[42:43], v[56:57], v[58:59] op_sel_hi:[0,1,1]
	v_cvt_pk_f32_fp8_e32 v[210:211], v240
	s_waitcnt vmcnt(9)
	v_pk_fma_f32 v[4:5], v[4:5], s[0:1], v[186:187] op_sel_hi:[1,0,1]
	v_cvt_pk_f32_fp8_sdwa v[186:187], v240 src0_sel:WORD_1
	v_pk_fma_f32 v[90:91], s[34:35], v[90:91], v[92:93] op_sel_hi:[0,1,1]
	v_pk_fma_f32 v[92:93], s[34:35], v[98:99], v[100:101] op_sel_hi:[0,1,1]
	v_pk_fma_f32 v[68:69], s[36:37], v[76:77], v[68:69] op_sel_hi:[0,1,1]
	v_pk_fma_f32 v[64:65], s[36:37], v[64:65], v[66:67] op_sel_hi:[0,1,1]
	v_pk_fma_f32 v[52:53], s[40:41], v[54:55], v[52:53] op_sel_hi:[0,1,1]
	v_pk_fma_f32 v[44:45], s[40:41], v[44:45], v[48:49] op_sel_hi:[0,1,1]
	v_cvt_pk_f32_fp8_e32 v[188:189], v245
	v_cvt_pk_f32_fp8_sdwa v[206:207], v245 src0_sel:WORD_1
	v_pk_fma_f32 v[92:93], s[30:31], v[94:95], v[92:93] op_sel_hi:[0,1,1]
	v_pk_fma_f32 v[88:89], s[30:31], v[88:89], v[90:91] op_sel_hi:[0,1,1]
	v_pk_fma_f32 v[62:63], s[34:35], v[62:63], v[64:65] op_sel_hi:[0,1,1]
	v_pk_fma_f32 v[64:65], s[34:35], v[74:75], v[68:69] op_sel_hi:[0,1,1]
	v_pk_fma_f32 v[40:41], s[38:39], v[40:41], v[44:45] op_sel_hi:[0,1,1]
	v_pk_fma_f32 v[44:45], s[38:39], v[50:51], v[52:53] op_sel_hi:[0,1,1]
	v_pk_fma_f32 v[6:7], v[6:7], s[0:1], v[194:195] op_sel_hi:[1,0,1]
	v_cvt_pk_f32_fp8_e32 v[194:195], v239
	v_cvt_pk_f32_fp8_sdwa v[226:227], v239 src0_sel:WORD_1
	v_pk_fma_f32 v[88:89], s[28:29], v[198:199], v[88:89] op_sel_hi:[0,1,1]
	v_pk_fma_f32 v[90:91], s[28:29], v[196:197], v[92:93] op_sel_hi:[0,1,1]
	v_pk_fma_f32 v[64:65], s[30:31], v[72:73], v[64:65] op_sel_hi:[0,1,1]
	v_pk_fma_f32 v[60:61], s[30:31], v[60:61], v[62:63] op_sel_hi:[0,1,1]
	v_pk_fma_f32 v[44:45], s[36:37], v[46:47], v[44:45] op_sel_hi:[0,1,1]
	v_pk_fma_f32 v[28:29], s[36:37], v[28:29], v[40:41] op_sel_hi:[0,1,1]
	v_pk_fma_f32 v[144:145], s[26:27], v[144:145], 0 op_sel_hi:[0,1,0]
	v_pk_fma_f32 v[138:139], s[26:27], v[138:139], 0 op_sel_hi:[0,1,0]
	s_waitcnt vmcnt(5)
; __device__ __forceinline__ void row_stats(const f32x4 (&v)[8], float& mean, float& rstd) {
;     float s = 0.f;
; #pragma unroll
;     for (int j = 0; j < 8; ++j) s += (v[j].x + v[j].y) + (v[j].z + v[j].w);
;     mean = wave_sum(s) * (1.f / DM);
; __device__ __forceinline__ void p9_row(const KA& a, int l, int row, const LAS int* pref, int lane, int ts_l, float w_l) {
;     ...
;     { const float w = 1.f / YS_SCALE;
; #pragma unroll
;         for (int j = 0; j < 8; ++j) { const f32x2 lo = __builtin_amdgcn_cvt_pk_f32_fp8(ys[j], false), hi = __builtin_amdgcn_cvt_pk_f32_fp8(ys[j], true);
;             m[j].x = fmaf(w, lo.x, m[j].x); m[j].y = fmaf(w, lo.y, m[j].y); m[j].z = fmaf(w, hi.x, m[j].z); m[j].w = fmaf(w, hi.y, m[j].w); } }
;     asm volatile("" ::: "memory");
;     f32x4 v[8];
; #pragma unroll
;     for (int j = 0; j < 8; ++j) { const f32x4 x1 = __builtin_nontemporal_load((const f32x4*)(X1 + (size_t)row * DM + 4 * lane + 256 * j)), g = *(const f32x4*)(gf + 4 * lane + 256 * j) + 1.0f;
;         v[j] = x1 * DN_ALPHA + g * m[j]; }
	v_pk_add_f32 v[10:11], v[10:11], 1.0 op_sel_hi:[1,0]
	v_pk_add_f32 v[8:9], v[8:9], 1.0 op_sel_hi:[1,0]
	v_pk_fma_f32 v[90:91], v[248:249], s[44:45], v[90:91] op_sel_hi:[1,0,1]
	v_pk_fma_f32 v[88:89], v[252:253], s[44:45], v[88:89] op_sel_hi:[1,0,1]
	v_pk_fma_f32 v[60:61], s[28:29], v[200:201], v[60:61] op_sel_hi:[0,1,1]
	v_pk_fma_f32 v[62:63], s[28:29], v[190:191], v[64:65] op_sel_hi:[0,1,1]
	v_pk_fma_f32 v[26:27], s[34:35], v[26:27], v[28:29] op_sel_hi:[0,1,1]
	v_pk_fma_f32 v[28:29], s[34:35], v[42:43], v[44:45] op_sel_hi:[0,1,1]
	v_pk_fma_f32 v[134:135], s[42:43], v[134:135], v[138:139] op_sel_hi:[0,1,1]
	v_pk_fma_f32 v[138:139], s[42:43], v[142:143], v[144:145] op_sel_hi:[0,1,1]
	v_pk_mul_f32 v[10:11], v[88:89], v[10:11]
	v_pk_mul_f32 v[8:9], v[90:91], v[8:9]
	s_waitcnt vmcnt(4)
	v_pk_add_f32 v[88:89], v[182:183], 1.0 op_sel_hi:[1,0]
	v_pk_add_f32 v[90:91], v[180:181], 1.0 op_sel_hi:[1,0]
	v_pk_fma_f32 v[62:63], v[210:211], s[44:45], v[62:63] op_sel_hi:[1,0,1]
	v_pk_fma_f32 v[60:61], v[186:187], s[44:45], v[60:61] op_sel_hi:[1,0,1]
	v_pk_fma_f32 v[28:29], s[30:31], v[30:31], v[28:29] op_sel_hi:[0,1,1]
	v_pk_fma_f32 v[24:25], s[30:31], v[24:25], v[26:27] op_sel_hi:[0,1,1]
	v_cvt_pk_f32_fp8_e32 v[184:185], v243
	v_cvt_pk_f32_fp8_sdwa v[244:245], v243 src0_sel:WORD_1
	v_pk_fma_f32 v[138:139], s[40:41], v[140:141], v[138:139] op_sel_hi:[0,1,1]
	v_pk_fma_f32 v[130:131], s[40:41], v[130:131], v[134:135] op_sel_hi:[0,1,1]
	v_pk_mul_f32 v[60:61], v[60:61], v[88:89]
	v_pk_mul_f32 v[64:65], v[62:63], v[90:91]
	v_pk_fma_f32 v[24:25], s[28:29], v[206:207], v[24:25] op_sel_hi:[0,1,1]
	v_pk_fma_f32 v[26:27], s[28:29], v[188:189], v[28:29] op_sel_hi:[0,1,1]
	v_pk_fma_f32 v[126:127], s[38:39], v[126:127], v[130:131] op_sel_hi:[0,1,1]
	v_pk_fma_f32 v[130:131], s[38:39], v[136:137], v[138:139] op_sel_hi:[0,1,1]
	s_waitcnt vmcnt(1)
	v_pk_fma_f32 v[62:63], v[150:151], s[0:1], v[60:61] op_sel_hi:[1,0,1]
	v_pk_fma_f32 v[60:61], v[148:149], s[0:1], v[64:65] op_sel_hi:[1,0,1]
	s_waitcnt vmcnt(0)
	v_pk_add_f32 v[64:65], v[154:155], 1.0 op_sel_hi:[1,0]
	v_pk_add_f32 v[66:67], v[152:153], 1.0 op_sel_hi:[1,0]
	v_pk_fma_f32 v[26:27], v[194:195], s[44:45], v[26:27] op_sel_hi:[1,0,1]
	v_pk_fma_f32 v[24:25], v[226:227], s[44:45], v[24:25] op_sel_hi:[1,0,1]
	v_cvt_pk_f32_fp8_e32 v[246:247], v242
	v_cvt_pk_f32_fp8_sdwa v[242:243], v242 src0_sel:WORD_1
	v_pk_fma_f32 v[130:131], s[36:37], v[132:133], v[130:131] op_sel_hi:[0,1,1]
	v_pk_fma_f32 v[122:123], s[36:37], v[122:123], v[126:127] op_sel_hi:[0,1,1]
	v_pk_mul_f32 v[24:25], v[24:25], v[64:65]
	v_pk_mul_f32 v[26:27], v[26:27], v[66:67]
	v_pk_fma_f32 v[116:117], s[28:29], v[208:209], v[146:147] op_sel_hi:[0,1,1]
	v_pk_fma_f32 v[120:121], s[34:35], v[120:121], v[122:123] op_sel_hi:[0,1,1]
	v_pk_fma_f32 v[122:123], s[34:35], v[128:129], v[130:131] op_sel_hi:[0,1,1]
	v_pk_fma_f32 v[40:41], v[18:19], s[0:1], v[24:25] op_sel_hi:[1,0,1]
	v_pk_fma_f32 v[42:43], v[16:17], s[0:1], v[26:27] op_sel_hi:[1,0,1]
	v_mov_b32_e32 v16, v22
	v_mov_b32_e32 v17, v12
	v_mov_b32_e32 v18, v23
	v_mov_b32_e32 v19, v13
	v_pk_add_f32 v[2:3], v[2:3], 1.0 op_sel_hi:[1,0]
	v_pk_add_f32 v[0:1], v[0:1], 1.0 op_sel_hi:[1,0]
	v_pk_fma_f32 v[116:117], v[244:245], s[44:45], v[116:117] op_sel_hi:[1,0,1]
	v_pk_fma_f32 v[146:147], v[184:185], s[44:45], v[156:157] op_sel_hi:[1,0,1]
	v_pk_fma_f32 v[122:123], s[30:31], v[124:125], v[122:123] op_sel_hi:[0,1,1]
	v_pk_fma_f32 v[118:119], s[30:31], v[118:119], v[120:121] op_sel_hi:[0,1,1]
	v_pk_add_f32 v[16:17], v[16:17], v[18:19]
	v_mov_b32_e32 v18, v20
	v_mov_b32_e32 v19, v14
	v_mov_b32_e32 v24, v21
	v_mov_b32_e32 v25, v15
	v_pk_mul_f32 v[0:1], v[146:147], v[0:1]
	v_pk_mul_f32 v[2:3], v[116:117], v[2:3]
	v_pk_fma_f32 v[118:119], s[28:29], v[202:203], v[118:119] op_sel_hi:[0,1,1]
	v_pk_fma_f32 v[120:121], s[28:29], v[250:251], v[122:123] op_sel_hi:[0,1,1]
	v_pk_add_f32 v[18:19], v[18:19], v[24:25]
	v_pk_fma_f32 v[146:147], v[218:219], s[0:1], v[2:3] op_sel_hi:[1,0,1]
	v_pk_fma_f32 v[116:117], v[216:217], s[0:1], v[0:1] op_sel_hi:[1,0,1]
	v_pk_add_f32 v[0:1], v[222:223], 1.0 op_sel_hi:[1,0]
	v_pk_add_f32 v[2:3], v[220:221], 1.0 op_sel_hi:[1,0]
	v_pk_fma_f32 v[120:121], v[246:247], s[44:45], v[120:121] op_sel_hi:[1,0,1]
	v_pk_fma_f32 v[118:119], v[242:243], s[44:45], v[118:119] op_sel_hi:[1,0,1]
	v_pk_add_f32 v[16:17], v[16:17], v[18:19]
	v_pk_mov_b32 v[18:19], v[4:5], v[6:7] op_sel:[1,0]
	v_mov_b32_e32 v24, v4
	v_mov_b32_e32 v25, v7
	v_pk_mul_f32 v[0:1], v[118:119], v[0:1]
	v_pk_mul_f32 v[118:119], v[120:121], v[2:3]
	v_pk_add_f32 v[18:19], v[18:19], v[24:25]
	v_pk_fma_f32 v[2:3], v[214:215], s[0:1], v[0:1] op_sel_hi:[1,0,1]
	v_pk_fma_f32 v[0:1], v[212:213], s[0:1], v[118:119] op_sel_hi:[1,0,1]
	v_add_f32_e32 v16, 0, v16
	v_pk_add_f32 v[18:19], v[18:19], v[18:19] op_sel:[0,1] op_sel_hi:[1,0]
	v_add_f32_e32 v16, v16, v17
	v_add_f32_e32 v24, v116, v117
	v_add_f32_e32 v26, v146, v147
	v_mov_b32_e32 v17, v0
	v_mov_b32_e32 v19, v1
	v_mov_b32_e32 v25, v2
	v_mov_b32_e32 v27, v3
	v_pk_fma_f32 v[10:11], v[178:179], s[0:1], v[10:11] op_sel_hi:[1,0,1]
	v_pk_fma_f32 v[8:9], v[176:177], s[0:1], v[8:9] op_sel_hi:[1,0,1]
	v_pk_add_f32 v[16:17], v[16:17], v[18:19]
	v_pk_add_f32 v[18:19], v[24:25], v[26:27]
	v_mov_b32_e32 v24, v8
	v_pk_add_f32 v[16:17], v[16:17], v[18:19]
	v_pk_mov_b32 v[18:19], v[8:9], v[10:11] op_sel:[1,0]
	v_mov_b32_e32 v25, v11
	v_pk_add_f32 v[18:19], v[18:19], v[24:25]
	v_pk_add_f32 v[16:17], v[16:17], v[16:17] op_sel:[0,1] op_sel_hi:[1,0]
	v_pk_add_f32 v[18:19], v[18:19], v[18:19] op_sel:[0,1] op_sel_hi:[1,0]
	v_add_f32_e32 v24, v60, v61
	v_add_f32_e32 v26, v62, v63
	v_mov_b32_e32 v17, v42
	v_mov_b32_e32 v19, v43
	v_mov_b32_e32 v25, v40
	v_mov_b32_e32 v27, v41
	v_pk_add_f32 v[16:17], v[16:17], v[18:19]
	v_pk_add_f32 v[18:19], v[24:25], v[26:27]
	s_load_dwordx4 s[44:47], s[8:9], 0xd0
	s_load_dwordx2 s[42:43], s[8:9], 0xe0
	v_pk_add_f32 v[16:17], v[16:17], v[18:19]
	v_mov_b32_e32 v227, 0x3727c5ac
	v_add_f32_e32 v16, v16, v17
	v_mov_b32_e32 v17, v193
	s_waitcnt lgkmcnt(0)
;     __device__ __forceinline__ const float* in(int i) const { return *(const float* const __attribute__((address_space(4)))*)(p + 8 * i); }
;     __device__ __forceinline__ float* out() const { return *(float* const __attribute__((address_space(4)))*)(p + 224); }
; __device__ __forceinline__ void row_stats(const f32x4 (&v)[8], float& mean, float& rstd) {
;     float s = 0.f;
; #pragma unroll
;     for (int j = 0; j < 8; ++j) s += (v[j].x + v[j].y) + (v[j].z + v[j].w);
;     mean = wave_sum(s) * (1.f / DM);
;     float s2 = 0.f;
; #pragma unroll
;     for (int j = 0; j < 8; ++j) { const f32x4 d = v[j] - mean; s2 += (d.x * d.x + d.y * d.y) + (d.z * d.z + d.w * d.w); }
;     rstd = rsqrtf(wave_sum(s2) * (1.f / DM) + LN_EPS);
; }
; __device__ __forceinline__ void p9_row(const KA& a, int l, int row, const LAS int* pref, int lane, int ts_l, float w_l) {
;     ...
;     float mean, rstd; row_stats(v, mean, rstd);
;     const float* g2 = a.in(26) + (size_t)l * DM; const float* b2 = a.in(27) + (size_t)l * DM;
;     asm volatile("" ::: "memory");
; #pragma unroll
;     for (int j = 0; j < 8; ++j) { const f32x4 g = *(const f32x4*)(g2 + 4 * lane + 256 * j), bb = *(const f32x4*)(b2 + 4 * lane + 256 * j);
;         v[j] = (v[j] - mean) * rstd * g + bb; *(f32x4*)(a.out() + (size_t)row * DM + 4 * lane + 256 * j) = v[j]; }
	s_add_u32 s0, s44, s22
	v_add_f32_dpp v16, v16, v16 row_shr:1 row_mask:0xf bank_mask:0xf bound_ctrl:1
	s_addc_u32 s1, s45, s23
	s_add_u32 s26, s46, s22
	v_add_f32_dpp v16, v16, v16 row_shr:2 row_mask:0xf bank_mask:0xf bound_ctrl:1
	s_addc_u32 s27, s47, s23
	v_mov_b32_e32 v231, 0x3a000000
	v_add_f32_dpp v16, v16, v16 row_shr:4 row_mask:0xf bank_mask:0xf bound_ctrl:1
	v_lshl_add_u64 v[50:51], s[26:27], 0, v[192:193]
	s_nop 0
	v_add_f32_dpp v16, v16, v16 row_shr:8 row_mask:0xf bank_mask:0xf bound_ctrl:1
	s_nop 1
	v_mov_b32_dpp v17, v16 row_bcast:15 row_mask:0xa bank_mask:0xf
	v_add_f32_e32 v16, v16, v17
	v_mov_b32_e32 v17, v193
	s_nop 1
	v_mov_b32_dpp v17, v16 row_bcast:31 row_mask:0xc bank_mask:0xf
	v_add_f32_e32 v16, v16, v17
	s_nop 0
	v_readlane_b32 s28, v16, 63
	s_nop 1
	v_fma_f32 v23, s28, v228, v23
	v_fma_f32 v13, s28, v228, v13
	v_fma_f32 v21, s28, v228, v21
	v_fmac_f32_e32 v22, s28, v228
	v_fma_f32 v15, s28, v228, v15
	v_fmac_f32_e32 v12, s28, v228
	v_mov_b32_e32 v18, v23
	v_mov_b32_e32 v19, v13
	v_fmac_f32_e32 v20, s28, v228
	v_fmac_f32_e32 v14, s28, v228
	v_mov_b32_e32 v16, v22
	v_mov_b32_e32 v17, v12
	v_pk_mul_f32 v[18:19], v[18:19], v[18:19]
	v_mov_b32_e32 v24, v21
	v_mov_b32_e32 v25, v15
	v_pk_fma_f32 v[16:17], v[16:17], v[16:17], v[18:19]
	v_mov_b32_e32 v18, v20
	v_mov_b32_e32 v19, v14
	v_pk_mul_f32 v[24:25], v[24:25], v[24:25]
	v_fma_f32 v5, s28, v228, v5
	v_pk_fma_f32 v[18:19], v[18:19], v[18:19], v[24:25]
	v_fmac_f32_e32 v4, s28, v228
	v_pk_add_f32 v[16:17], v[16:17], v[18:19]
	v_fma_f32 v7, s28, v228, v7
	v_pk_add_f32 v[28:29], v[16:17], v[16:17] op_sel_hi:[0,1]
	global_load_dwordx4 v[16:19], v192, s[0:1]
	global_load_dwordx4 v[24:27], v192, s[26:27]
	v_fmac_f32_e32 v6, s28, v228
	v_pk_mul_f32 v[30:31], v[6:7], v[6:7]
	v_pk_mul_f32 v[44:45], v[4:5], v[4:5]
	v_fmac_f32_e32 v116, s28, v228
	v_pk_mov_b32 v[46:47], v[44:45], v[30:31] op_sel:[1,0]
	v_mov_b32_e32 v45, v31
	v_fma_f32 v117, s28, v228, v117
	v_fmac_f32_e32 v146, s28, v228
	v_mul_f32_e32 v28, v116, v116
	v_pk_add_f32 v[30:31], v[46:47], v[44:45]
	v_fma_f32 v147, s28, v228, v147
	v_pk_fma_f32 v[44:45], v[116:117], v[116:117], v[28:29] op_sel_hi:[1,1,0]
	v_mul_f32_e32 v28, v146, v146
	v_pk_add_f32 v[30:31], v[30:31], v[30:31] op_sel_hi:[0,1]
	v_pk_fma_f32 v[46:47], v[146:147], v[146:147], v[28:29] op_sel_hi:[1,1,0]
	v_fma_f32 v3, s28, v228, v3
	v_fmac_f32_e32 v2, s28, v228
	v_fma_f32 v1, s28, v228, v1
	v_fmac_f32_e32 v0, s28, v228
	v_mul_f32_e32 v44, v0, v0
	v_mul_f32_e32 v46, v1, v1
	v_mul_f32_e32 v30, v2, v2
	v_mul_f32_e32 v28, v3, v3
	v_pk_add_f32 v[44:45], v[44:45], v[46:47]
	v_pk_add_f32 v[28:29], v[30:31], v[28:29]
	v_fma_f32 v9, s28, v228, v9
	v_pk_add_f32 v[28:29], v[44:45], v[28:29]
	v_fmac_f32_e32 v8, s28, v228
	v_fma_f32 v11, s28, v228, v11
	v_fmac_f32_e32 v10, s28, v228
	v_pk_add_f32 v[28:29], v[28:29], v[28:29] op_sel_hi:[0,1]
	v_pk_mul_f32 v[30:31], v[10:11], v[10:11]
	v_pk_mul_f32 v[44:45], v[8:9], v[8:9]
	v_fmac_f32_e32 v60, s28, v228
	v_pk_mov_b32 v[46:47], v[44:45], v[30:31] op_sel:[1,0]
	v_mov_b32_e32 v45, v31
	v_fma_f32 v61, s28, v228, v61
	v_fmac_f32_e32 v62, s28, v228
	v_mul_f32_e32 v28, v60, v60
	v_pk_add_f32 v[30:31], v[46:47], v[44:45]
	v_fma_f32 v63, s28, v228, v63
	v_pk_fma_f32 v[44:45], v[60:61], v[60:61], v[28:29] op_sel_hi:[1,1,0]
	v_mul_f32_e32 v28, v62, v62
	v_pk_add_f32 v[30:31], v[30:31], v[30:31] op_sel_hi:[0,1]
	v_pk_fma_f32 v[46:47], v[62:63], v[62:63], v[28:29] op_sel_hi:[1,1,0]
	v_fma_f32 v41, s28, v228, v41
	v_fmac_f32_e32 v40, s28, v228
	v_fma_f32 v43, s28, v228, v43
	v_fmac_f32_e32 v42, s28, v228
	v_mul_f32_e32 v44, v42, v42
	v_mul_f32_e32 v46, v43, v43
	v_mul_f32_e32 v30, v40, v40
	v_mul_f32_e32 v28, v41, v41
	v_pk_add_f32 v[44:45], v[44:45], v[46:47]
	v_pk_add_f32 v[28:29], v[30:31], v[28:29]
	v_lshl_add_u64 v[46:47], s[0:1], 0, v[192:193]
	v_pk_add_f32 v[28:29], v[44:45], v[28:29]
	v_lshl_add_u64 v[44:45], s[42:43], 0, v[38:39]
	v_add_f32_e32 v28, v28, v29
	v_mov_b32_e32 v29, v193
	s_nop 0
	v_add_f32_dpp v28, v28, v28 row_shr:1 row_mask:0xf bank_mask:0xf bound_ctrl:1
	s_nop 1
	v_add_f32_dpp v28, v28, v28 row_shr:2 row_mask:0xf bank_mask:0xf bound_ctrl:1
	s_nop 1
	v_add_f32_dpp v28, v28, v28 row_shr:4 row_mask:0xf bank_mask:0xf bound_ctrl:1
	s_nop 1
	v_add_f32_dpp v28, v28, v28 row_shr:8 row_mask:0xf bank_mask:0xf bound_ctrl:1
	s_nop 1
	v_mov_b32_dpp v29, v28 row_bcast:15 row_mask:0xa bank_mask:0xf
	v_add_f32_e32 v28, v28, v29
	v_mov_b32_e32 v29, v193
	s_nop 1
	v_mov_b32_dpp v29, v28 row_bcast:31 row_mask:0xc bank_mask:0xf
	v_add_f32_e32 v28, v28, v29
	s_nop 0
	v_readlane_b32 s28, v28, 63
	s_nop 1
	v_fma_f32 v28, s28, v231, v227
	s_mov_b32 s28, 0x800000
	v_mul_f32_e32 v29, 0x4b800000, v28
	v_cmp_gt_f32_e32 vcc, s28, v28
	s_nop 1
	v_cndmask_b32_e32 v28, v28, v29, vcc
	v_rsq_f32_e32 v28, v28
	s_nop 0
	v_mul_f32_e32 v29, 0x45800000, v28
	v_cndmask_b32_e32 v48, v28, v29, vcc
	v_pk_mul_f32 v[22:23], v[22:23], v[48:49] op_sel_hi:[1,0]
	v_pk_mul_f32 v[20:21], v[20:21], v[48:49] op_sel_hi:[1,0]
	s_waitcnt vmcnt(0)
	v_pk_fma_f32 v[28:29], v[16:17], v[22:23], v[24:25]
	v_pk_fma_f32 v[30:31], v[18:19], v[20:21], v[26:27]
	global_store_dwordx4 v[44:45], v[28:31], off nt
	global_load_dwordx4 v[16:19], v192, s[0:1] offset:1024
	global_load_dwordx4 v[20:23], v192, s[26:27] offset:1024
	v_pk_mul_f32 v[14:15], v[14:15], v[48:49] op_sel_hi:[1,0]
	v_pk_mul_f32 v[12:13], v[12:13], v[48:49] op_sel_hi:[1,0]
	v_pk_mul_f32 v[6:7], v[6:7], v[48:49] op_sel_hi:[1,0]
	v_pk_mul_f32 v[4:5], v[4:5], v[48:49] op_sel_hi:[1,0]
	v_pk_mul_f32 v[2:3], v[2:3], v[48:49] op_sel_hi:[1,0]
	v_pk_mul_f32 v[0:1], v[0:1], v[48:49] op_sel_hi:[1,0]
	v_pk_mul_f32 v[10:11], v[10:11], v[48:49] op_sel_hi:[1,0]
	v_pk_mul_f32 v[8:9], v[8:9], v[48:49] op_sel_hi:[1,0]
	v_pk_mul_f32 v[54:55], v[60:61], v[48:49] op_sel_hi:[1,0]
	v_pk_mul_f32 v[40:41], v[40:41], v[48:49] op_sel_hi:[1,0]
	v_pk_mul_f32 v[42:43], v[42:43], v[48:49] op_sel_hi:[1,0]
	s_waitcnt vmcnt(0)
;     __device__ __forceinline__ float* out() const { return *(float* const __attribute__((address_space(4)))*)(p + 224); }
;     __device__ __forceinline__ unsigned char* ws() const { return *(unsigned char* const __attribute__((address_space(4)))*)(p + 232); }
; __device__ __forceinline__ void row_stats(const f32x4 (&v)[8], float& mean, float& rstd) {
;     float s = 0.f;
; #pragma unroll
;     for (int j = 0; j < 8; ++j) s += (v[j].x + v[j].y) + (v[j].z + v[j].w);
;     mean = wave_sum(s) * (1.f / DM);
;     float s2 = 0.f;
; #pragma unroll
;     for (int j = 0; j < 8; ++j) { const f32x4 d = v[j] - mean; s2 += (d.x * d.x + d.y * d.y) + (d.z * d.z + d.w * d.w); }
;     rstd = rsqrtf(wave_sum(s2) * (1.f / DM) + LN_EPS);
; }
; __device__ __forceinline__ void p9_row(const KA& a, int l, int row, const LAS int* pref, int lane, int ts_l, float w_l) {
;     ...
;     for (int j = 0; j < 8; ++j) { const f32x4 g = *(const f32x4*)(g2 + 4 * lane + 256 * j), bb = *(const f32x4*)(b2 + 4 * lane + 256 * j);
;         v[j] = (v[j] - mean) * rstd * g + bb; *(f32x4*)(a.out() + (size_t)row * DM + 4 * lane + 256 * j) = v[j]; }
;     asm volatile("" ::: "memory");
;     if (l + 1 < NLAYER) {
;         const float* ada2 = (const float*)(ws + WS_ADA) + (size_t)((l + 1) * 2 + b) * ADA_W;
;         row_stats(v, mean, rstd);
	v_pk_fma_f32 v[24:25], v[16:17], v[12:13], v[20:21]
	v_pk_fma_f32 v[26:27], v[18:19], v[14:15], v[22:23]
	global_store_dwordx4 v[44:45], v[24:27], off offset:1024 nt
	global_load_dwordx4 v[12:15], v192, s[0:1] offset:2048
	global_load_dwordx4 v[16:19], v192, s[26:27] offset:2048
	s_waitcnt vmcnt(0)
	v_pk_fma_f32 v[20:21], v[4:5], v[12:13], v[16:17]
	v_pk_fma_f32 v[22:23], v[6:7], v[14:15], v[18:19]
	global_store_dwordx4 v[44:45], v[20:23], off offset:2048 nt
	global_load_dwordx4 v[4:7], v192, s[0:1] offset:3072
	global_load_dwordx4 v[12:15], v192, s[26:27] offset:3072
	s_movk_i32 s0, 0x1000
	v_add_co_u32_e32 v46, vcc, s0, v46
	v_pk_mul_f32 v[18:19], v[146:147], v[48:49] op_sel_hi:[1,0]
	v_pk_mul_f32 v[16:17], v[116:117], v[48:49] op_sel_hi:[1,0]
	v_addc_co_u32_e32 v47, vcc, 0, v47, vcc
	v_add_co_u32_e32 v50, vcc, s0, v50
	s_waitcnt vmcnt(0)
	v_pk_fma_f32 v[16:17], v[16:17], v[4:5], v[12:13]
	v_pk_fma_f32 v[18:19], v[18:19], v[6:7], v[14:15]
	global_store_dwordx4 v[44:45], v[16:19], off offset:3072 nt
	v_addc_co_u32_e32 v51, vcc, 0, v51, vcc
	global_load_dwordx4 v[4:7], v[46:47], off
	global_load_dwordx4 v[12:15], v[50:51], off
	v_add_co_u32_e32 v52, vcc, s0, v44
	v_readlane_b32 s0, v254, 41
	s_nop 0
	v_addc_co_u32_e32 v53, vcc, 0, v45, vcc
	v_pk_mul_f32 v[44:45], v[62:63], v[48:49] op_sel_hi:[1,0]
	v_readlane_b32 s1, v254, 42
	s_andn2_b64 vcc, exec, s[0:1]
	s_waitcnt vmcnt(0)
	v_pk_fma_f32 v[12:13], v[0:1], v[4:5], v[12:13]
	v_pk_fma_f32 v[14:15], v[2:3], v[6:7], v[14:15]
	global_store_dwordx4 v[52:53], v[12:15], off nt
	global_load_dwordx4 v[0:3], v[46:47], off offset:1024
	global_load_dwordx4 v[4:7], v[50:51], off offset:1024
	s_waitcnt vmcnt(0)
	v_pk_fma_f32 v[8:9], v[8:9], v[0:1], v[4:5]
	v_pk_fma_f32 v[10:11], v[10:11], v[2:3], v[6:7]
	global_store_dwordx4 v[52:53], v[8:11], off offset:1024 nt
	global_load_dwordx4 v[0:3], v[46:47], off offset:2048
	global_load_dwordx4 v[4:7], v[50:51], off offset:2048
	s_waitcnt vmcnt(0)
	v_pk_fma_f32 v[4:5], v[54:55], v[0:1], v[4:5]
	v_pk_fma_f32 v[6:7], v[44:45], v[2:3], v[6:7]
	global_store_dwordx4 v[52:53], v[4:7], off offset:2048 nt
	global_load_dwordx4 v[0:3], v[46:47], off offset:3072
	s_nop 0
	global_load_dwordx4 v[44:47], v[50:51], off offset:3072
	s_waitcnt vmcnt(0)
	v_pk_fma_f32 v[0:1], v[42:43], v[0:1], v[44:45]
	v_pk_fma_f32 v[2:3], v[40:41], v[2:3], v[46:47]
	global_store_dwordx4 v[52:53], v[0:3], off offset:3072 nt
	s_cbranch_vccnz .LBB0_1653
	v_mov_b32_e32 v40, v24
	v_mov_b32_e32 v41, v28
	v_mov_b32_e32 v42, v25
	v_mov_b32_e32 v43, v29
	v_pk_add_f32 v[40:41], v[40:41], v[42:43]
	v_mov_b32_e32 v42, v26
	v_mov_b32_e32 v43, v30
	v_mov_b32_e32 v44, v27
	v_mov_b32_e32 v45, v31
	v_pk_add_f32 v[42:43], v[42:43], v[44:45]
	v_mov_b32_e32 v44, v20
	v_pk_add_f32 v[40:41], v[40:41], v[42:43]
	v_mov_b32_e32 v42, v21
	v_mov_b32_e32 v43, v22
	v_mov_b32_e32 v45, v23
	v_pk_add_f32 v[42:43], v[42:43], v[44:45]
	v_add_f32_e32 v41, 0, v41
	v_pk_add_f32 v[42:43], v[42:43], v[42:43] op_sel:[0,1] op_sel_hi:[1,0]
	v_add_f32_e32 v40, v40, v41
	v_add_f32_e32 v44, v16, v17
	v_add_f32_e32 v46, v18, v19
	v_mov_b32_e32 v43, v12
	v_mov_b32_e32 v41, v13
	v_mov_b32_e32 v45, v14
	v_mov_b32_e32 v47, v15
	v_pk_add_f32 v[40:41], v[42:43], v[40:41]
	v_pk_add_f32 v[42:43], v[44:45], v[46:47]
	v_mov_b32_e32 v44, v8
	v_pk_add_f32 v[40:41], v[40:41], v[42:43]
	v_mov_b32_e32 v42, v9
	v_mov_b32_e32 v43, v10
	v_mov_b32_e32 v45, v11
	v_pk_add_f32 v[42:43], v[42:43], v[44:45]
	v_pk_add_f32 v[40:41], v[40:41], v[40:41] op_sel:[0,1] op_sel_hi:[1,0]
	v_pk_add_f32 v[42:43], v[42:43], v[42:43] op_sel:[0,1] op_sel_hi:[1,0]
	v_add_f32_e32 v44, v4, v5
	v_add_f32_e32 v46, v6, v7
	v_mov_b32_e32 v41, v0
	v_mov_b32_e32 v43, v1
	v_mov_b32_e32 v45, v2
	v_mov_b32_e32 v47, v3
	v_pk_add_f32 v[40:41], v[40:41], v[42:43]
	v_pk_add_f32 v[42:43], v[44:45], v[46:47]
	s_add_i32 s0, s41, 2
	v_pk_add_f32 v[40:41], v[40:41], v[42:43]
	s_mul_hi_i32 s1, s0, 0xc000
	v_add_f32_e32 v40, v40, v41
	v_mov_b32_e32 v41, v193
	s_mul_i32 s0, s0, 0xc000
	v_add_f32_dpp v40, v40, v40 row_shr:1 row_mask:0xf bank_mask:0xf bound_ctrl:1
	s_add_u32 s26, s31, s0
	s_addc_u32 s27, s35, s1
	v_add_f32_dpp v40, v40, v40 row_shr:2 row_mask:0xf bank_mask:0xf bound_ctrl:1
	v_lshl_add_u64 v[52:53], s[10:11], 0, v[36:37]
	s_nop 0
	v_add_f32_dpp v40, v40, v40 row_shr:4 row_mask:0xf bank_mask:0xf bound_ctrl:1
	s_nop 1
	v_add_f32_dpp v40, v40, v40 row_shr:8 row_mask:0xf bank_mask:0xf bound_ctrl:1
	s_nop 1
	v_mov_b32_dpp v41, v40 row_bcast:15 row_mask:0xa bank_mask:0xf
	v_add_f32_e32 v40, v40, v41
	v_mov_b32_e32 v41, v193
	s_nop 1
	v_mov_b32_dpp v41, v40 row_bcast:31 row_mask:0xc bank_mask:0xf
	v_add_f32_e32 v40, v40, v41
	s_nop 0
	v_readlane_b32 s0, v40, 63
	s_nop 1
	v_fma_f32 v29, s0, v228, v29
	v_fma_f32 v25, s0, v228, v25
	v_fma_f32 v45, s0, v228, v31
	v_fma_f32 v44, s0, v228, v30
	v_fmac_f32_e32 v28, s0, v228
	v_fma_f32 v43, s0, v228, v27
	v_fmac_f32_e32 v24, s0, v228
	v_mov_b32_e32 v30, v29
	v_mov_b32_e32 v31, v25
	v_fma_f32 v42, s0, v228, v26
	v_mov_b32_e32 v26, v28
	v_mov_b32_e32 v27, v24
	v_pk_mul_f32 v[30:31], v[30:31], v[30:31]
	v_mov_b32_e32 v40, v45
	v_mov_b32_e32 v41, v43
	v_pk_fma_f32 v[26:27], v[26:27], v[26:27], v[30:31]
	v_mov_b32_e32 v30, v44
	v_mov_b32_e32 v31, v42
	v_pk_mul_f32 v[40:41], v[40:41], v[40:41]
	v_fma_f32 v23, s0, v228, v23
	v_pk_fma_f32 v[30:31], v[30:31], v[30:31], v[40:41]
	v_fma_f32 v41, s0, v228, v21
	v_pk_add_f32 v[26:27], v[26:27], v[30:31]
	v_fma_f32 v40, s0, v228, v20
	v_fmac_f32_e32 v22, s0, v228
	v_pk_add_f32 v[46:47], v[26:27], v[26:27] op_sel_hi:[0,1]
	v_pk_mul_f32 v[20:21], v[22:23], v[22:23]
	v_pk_mul_f32 v[26:27], v[40:41], v[40:41]
;     __device__ __forceinline__ unsigned char* ws() const { return *(unsigned char* const __attribute__((address_space(4)))*)(p + 232); }
; __device__ __forceinline__ void row_stats(const f32x4 (&v)[8], float& mean, float& rstd) {
;     float s = 0.f;
; #pragma unroll
;     for (int j = 0; j < 8; ++j) s += (v[j].x + v[j].y) + (v[j].z + v[j].w);
;     mean = wave_sum(s) * (1.f / DM);
;     float s2 = 0.f;
; #pragma unroll
;     for (int j = 0; j < 8; ++j) { const f32x4 d = v[j] - mean; s2 += (d.x * d.x + d.y * d.y) + (d.z * d.z + d.w * d.w); }
;     rstd = rsqrtf(wave_sum(s2) * (1.f / DM) + LN_EPS);
; }
; __device__ __forceinline__ void p9_row(const KA& a, int l, int row, const LAS int* pref, int lane, int ts_l, float w_l) {
;     ...
;         row_stats(v, mean, rstd);
;         bf16* hrow = (bf16*)(ws + WS_H) + (size_t)row * DM;
; #pragma unroll
;         for (int j = 0; j < 8; ++j) { const f32x4 s1 = *(const f32x4*)(ada2 + DM + 4 * lane + 256 * j) + 1.0f, s0 = *(const f32x4*)(ada2 + 4 * lane + 256 * j);
;             const f32x4 y = (v[j] - mean) * rstd * s1 + s0;
	v_fmac_f32_e32 v18, s0, v228
	v_pk_mov_b32 v[30:31], v[26:27], v[20:21] op_sel:[1,0]
	v_mov_b32_e32 v27, v21
	v_pk_add_f32 v[20:21], v[30:31], v[26:27]
	v_fma_f32 v30, s0, v228, v16
	v_fma_f32 v31, s0, v228, v17
	v_mul_f32_e32 v16, v30, v30
	v_pk_fma_f32 v[16:17], v[30:31], v[30:31], v[16:17] op_sel_hi:[1,1,0]
	v_fma_f32 v19, s0, v228, v19
	v_mul_f32_e32 v16, v18, v18
	v_pk_add_f32 v[20:21], v[20:21], v[20:21] op_sel_hi:[0,1]
	v_pk_fma_f32 v[48:49], v[18:19], v[18:19], v[16:17] op_sel_hi:[1,1,0]
	v_fma_f32 v27, s0, v228, v15
	v_fma_f32 v26, s0, v228, v14
	v_fma_f32 v13, s0, v228, v13
	v_fmac_f32_e32 v12, s0, v228
	v_mul_f32_e32 v16, v12, v12
	v_mul_f32_e32 v48, v13, v13
	v_mul_f32_e32 v20, v26, v26
	v_mul_f32_e32 v46, v27, v27
	v_pk_add_f32 v[14:15], v[16:17], v[48:49]
	v_pk_add_f32 v[16:17], v[20:21], v[46:47]
	v_fma_f32 v21, s0, v228, v9
	v_fma_f32 v20, s0, v228, v8
	v_fma_f32 v11, s0, v228, v11
	v_fmac_f32_e32 v10, s0, v228
	v_pk_add_f32 v[14:15], v[14:15], v[16:17]
	v_pk_mul_f32 v[8:9], v[10:11], v[10:11]
	v_pk_mul_f32 v[16:17], v[20:21], v[20:21]
	v_fmac_f32_e32 v6, s0, v228
	v_pk_mov_b32 v[46:47], v[16:17], v[8:9] op_sel:[1,0]
	v_mov_b32_e32 v17, v9
	v_pk_add_f32 v[8:9], v[46:47], v[16:17]
	v_fma_f32 v16, s0, v228, v4
	v_fma_f32 v17, s0, v228, v5
	v_mul_f32_e32 v4, v16, v16
	v_pk_fma_f32 v[4:5], v[16:17], v[16:17], v[4:5] op_sel_hi:[1,1,0]
	v_fma_f32 v7, s0, v228, v7
	v_mul_f32_e32 v4, v6, v6
	v_pk_add_f32 v[14:15], v[14:15], v[14:15] op_sel_hi:[0,1]
	v_pk_add_f32 v[46:47], v[8:9], v[8:9] op_sel_hi:[0,1]
	v_pk_fma_f32 v[48:49], v[6:7], v[6:7], v[4:5] op_sel_hi:[1,1,0]
	v_fma_f32 v9, s0, v228, v3
	v_fma_f32 v8, s0, v228, v2
	v_fma_f32 v1, s0, v228, v1
	v_fmac_f32_e32 v0, s0, v228
	v_mul_f32_e32 v4, v0, v0
	v_mul_f32_e32 v48, v1, v1
	v_mul_f32_e32 v46, v8, v8
	v_mul_f32_e32 v14, v9, v9
	v_pk_add_f32 v[2:3], v[4:5], v[48:49]
	v_pk_add_f32 v[4:5], v[46:47], v[14:15]
	v_lshl_add_u64 v[48:49], s[26:27], 0, v[192:193]
	v_pk_add_f32 v[2:3], v[2:3], v[4:5]
	s_nop 0
	v_add_f32_e32 v2, v2, v3
	v_mov_b32_e32 v3, v193
	s_nop 0
	v_add_f32_dpp v2, v2, v2 row_shr:1 row_mask:0xf bank_mask:0xf bound_ctrl:1
	s_nop 1
	v_add_f32_dpp v2, v2, v2 row_shr:2 row_mask:0xf bank_mask:0xf bound_ctrl:1
	s_nop 1
	v_add_f32_dpp v2, v2, v2 row_shr:4 row_mask:0xf bank_mask:0xf bound_ctrl:1
	s_nop 1
	v_add_f32_dpp v2, v2, v2 row_shr:8 row_mask:0xf bank_mask:0xf bound_ctrl:1
	s_nop 1
	v_mov_b32_dpp v3, v2 row_bcast:15 row_mask:0xa bank_mask:0xf
	v_add_f32_e32 v2, v2, v3
	v_mov_b32_e32 v3, v193
	s_nop 1
	v_mov_b32_dpp v3, v2 row_bcast:31 row_mask:0xc bank_mask:0xf
	v_add_f32_e32 v2, v2, v3
	s_nop 0
	v_readlane_b32 s0, v2, 63
	s_nop 1
	v_fma_f32 v2, s0, v231, v227
	v_cmp_gt_f32_e32 vcc, s28, v2
	v_mul_f32_e32 v3, 0x4b800000, v2
	s_mov_b64 s[0:1], 0x2000
	v_cndmask_b32_e32 v2, v2, v3, vcc
	v_rsq_f32_e32 v2, v2
	v_lshl_add_u64 v[50:51], v[48:49], 0, s[0:1]
	s_movk_i32 s0, 0x3000
	v_mul_f32_e32 v3, 0x45800000, v2
	v_cndmask_b32_e32 v14, v2, v3, vcc
	v_add_co_u32_e32 v46, vcc, s0, v48
	v_pk_mul_f32 v[28:29], v[28:29], v[14:15] op_sel_hi:[1,0]
	s_nop 0
	v_addc_co_u32_e32 v47, vcc, 0, v49, vcc
	global_load_dwordx4 v[2:5], v[46:47], off offset:-4096
	v_pk_mul_f32 v[44:45], v[44:45], v[14:15] op_sel_hi:[1,0]
	v_pk_mul_f32 v[24:25], v[24:25], v[14:15] op_sel_hi:[1,0]
	v_pk_mul_f32 v[42:43], v[42:43], v[14:15] op_sel_hi:[1,0]
	v_pk_mul_f32 v[22:23], v[22:23], v[14:15] op_sel_hi:[1,0]
	v_pk_mul_f32 v[30:31], v[30:31], v[14:15] op_sel_hi:[1,0]
	v_pk_mul_f32 v[18:19], v[18:19], v[14:15] op_sel_hi:[1,0]
	s_movk_i32 s0, 0x1000
	v_pk_mul_f32 v[12:13], v[12:13], v[14:15] op_sel_hi:[1,0]
	v_pk_mul_f32 v[26:27], v[26:27], v[14:15] op_sel_hi:[1,0]
	v_pk_mul_f32 v[10:11], v[10:11], v[14:15] op_sel_hi:[1,0]
	v_pk_mul_f32 v[16:17], v[16:17], v[14:15] op_sel_hi:[1,0]
	v_pk_mul_f32 v[6:7], v[6:7], v[14:15] op_sel_hi:[1,0]
	v_pk_mul_f32 v[0:1], v[0:1], v[14:15] op_sel_hi:[1,0]
	v_pk_mul_f32 v[8:9], v[8:9], v[14:15] op_sel_hi:[1,0]
	s_waitcnt vmcnt(0)
; __device__ __forceinline__ unsigned cvt_pk_bf16(float lo, float hi) { unsigned r; asm volatile("v_cvt_pk_bf16_f32 %0, %1, %2" : "=v"(r) : "v"(lo), "v"(hi)); return r; }
; __device__ __forceinline__ void p9_row(const KA& a, int l, int row, const LAS int* pref, int lane, int ts_l, float w_l) {
;     ...
; #pragma unroll
;         for (int j = 0; j < 8; ++j) { const f32x4 s1 = *(const f32x4*)(ada2 + DM + 4 * lane + 256 * j) + 1.0f, s0 = *(const f32x4*)(ada2 + 4 * lane + 256 * j);
;             const f32x4 y = (v[j] - mean) * rstd * s1 + s0;
;             u32x2 w; w.x = cvt_pk_bf16(y.x, y.y); w.y = cvt_pk_bf16(y.z, y.w); *(u32x2*)(hrow + 4 * lane + 256 * j) = w; }
	v_pk_add_f32 v[54:55], v[4:5], 1.0 op_sel_hi:[1,0]
	v_pk_add_f32 v[56:57], v[2:3], 1.0 op_sel_hi:[1,0]
	global_load_dwordx4 v[2:5], v192, s[26:27]
	s_waitcnt vmcnt(0)
	v_pk_fma_f32 v[2:3], v[56:57], v[28:29], v[2:3]
	s_nop 0
	v_cvt_pk_bf16_f32 v28, v2, v3
	v_add_co_u32_e32 v2, vcc, s28, v52
	v_pk_fma_f32 v[4:5], v[54:55], v[44:45], v[4:5]
	s_nop 0
	v_addc_co_u32_e32 v3, vcc, 0, v53, vcc
	v_cvt_pk_bf16_f32 v29, v4, v5
	global_store_dwordx2 v[2:3], v[28:29], off
	global_load_dwordx4 v[52:55], v[50:51], off offset:1024
	s_waitcnt vmcnt(0)
	v_pk_add_f32 v[4:5], v[54:55], 1.0 op_sel_hi:[1,0]
	v_pk_add_f32 v[28:29], v[52:53], 1.0 op_sel_hi:[1,0]
	global_load_dwordx4 v[52:55], v192, s[26:27] offset:1024
	s_waitcnt vmcnt(0)
	v_pk_fma_f32 v[24:25], v[28:29], v[24:25], v[52:53]
	v_pk_fma_f32 v[4:5], v[4:5], v[42:43], v[54:55]
	v_cvt_pk_bf16_f32 v24, v24, v25
	v_pk_mul_f32 v[28:29], v[40:41], v[14:15] op_sel_hi:[1,0]
	v_cvt_pk_bf16_f32 v25, v4, v5
	global_store_dwordx2 v[2:3], v[24:25], off offset:512
	global_load_dwordx4 v[42:45], v[50:51], off offset:2048
	s_waitcnt vmcnt(0)
	v_pk_add_f32 v[4:5], v[44:45], 1.0 op_sel_hi:[1,0]
	v_pk_add_f32 v[24:25], v[42:43], 1.0 op_sel_hi:[1,0]
	global_load_dwordx4 v[42:45], v192, s[26:27] offset:2048
	s_waitcnt vmcnt(0)
	v_pk_fma_f32 v[4:5], v[22:23], v[4:5], v[44:45]
	v_pk_fma_f32 v[22:23], v[28:29], v[24:25], v[42:43]
	s_nop 0
	v_cvt_pk_bf16_f32 v22, v22, v23
	v_cvt_pk_bf16_f32 v23, v4, v5
	global_store_dwordx2 v[2:3], v[22:23], off offset:1024
	global_load_dwordx4 v[22:25], v[50:51], off offset:3072
	s_waitcnt vmcnt(0)
	v_pk_add_f32 v[4:5], v[24:25], 1.0 op_sel_hi:[1,0]
	v_pk_add_f32 v[28:29], v[22:23], 1.0 op_sel_hi:[1,0]
	global_load_dwordx4 v[22:25], v192, s[26:27] offset:3072
	s_waitcnt vmcnt(0)
	v_pk_fma_f32 v[4:5], v[18:19], v[4:5], v[24:25]
	v_pk_fma_f32 v[18:19], v[30:31], v[28:29], v[22:23]
	v_add_co_u32_e32 v28, vcc, s0, v48
	v_cvt_pk_bf16_f32 v18, v18, v19
	v_cvt_pk_bf16_f32 v19, v4, v5
	global_store_dwordx2 v[2:3], v[18:19], off offset:1536
	global_load_dwordx4 v[22:25], v[46:47], off
	v_addc_co_u32_e32 v29, vcc, 0, v49, vcc
	s_waitcnt vmcnt(0)
	v_pk_add_f32 v[4:5], v[24:25], 1.0 op_sel_hi:[1,0]
	v_pk_add_f32 v[18:19], v[22:23], 1.0 op_sel_hi:[1,0]
	global_load_dwordx4 v[22:25], v[28:29], off
	s_waitcnt vmcnt(0)
	v_pk_fma_f32 v[12:13], v[12:13], v[18:19], v[22:23]
	v_pk_fma_f32 v[4:5], v[26:27], v[4:5], v[24:25]
	v_cvt_pk_bf16_f32 v12, v12, v13
	v_pk_mul_f32 v[18:19], v[20:21], v[14:15] op_sel_hi:[1,0]
	v_cvt_pk_bf16_f32 v13, v4, v5
	global_store_dwordx2 v[2:3], v[12:13], off offset:2048
	global_load_dwordx4 v[22:25], v[46:47], off offset:1024
	s_waitcnt vmcnt(0)
	v_pk_add_f32 v[4:5], v[24:25], 1.0 op_sel_hi:[1,0]
	v_pk_add_f32 v[12:13], v[22:23], 1.0 op_sel_hi:[1,0]
	global_load_dwordx4 v[22:25], v[28:29], off offset:1024
	s_waitcnt vmcnt(0)
	v_pk_fma_f32 v[4:5], v[10:11], v[4:5], v[24:25]
	v_pk_fma_f32 v[10:11], v[18:19], v[12:13], v[22:23]
	s_nop 0
	v_cvt_pk_bf16_f32 v10, v10, v11
	v_cvt_pk_bf16_f32 v11, v4, v5
	global_store_dwordx2 v[2:3], v[10:11], off offset:2560
	global_load_dwordx4 v[10:13], v[46:47], off offset:2048
	s_waitcnt vmcnt(0)
	v_pk_add_f32 v[4:5], v[12:13], 1.0 op_sel_hi:[1,0]
	v_pk_add_f32 v[18:19], v[10:11], 1.0 op_sel_hi:[1,0]
	global_load_dwordx4 v[10:13], v[28:29], off offset:2048
	s_waitcnt vmcnt(0)
	v_pk_fma_f32 v[4:5], v[6:7], v[4:5], v[12:13]
	v_pk_fma_f32 v[6:7], v[16:17], v[18:19], v[10:11]
	s_nop 0
	v_cvt_pk_bf16_f32 v6, v6, v7
	v_cvt_pk_bf16_f32 v7, v4, v5
	global_store_dwordx2 v[2:3], v[6:7], off offset:3072
	global_load_dwordx4 v[4:7], v[46:47], off offset:3072
	s_waitcnt vmcnt(0)
	v_pk_add_f32 v[10:11], v[6:7], 1.0 op_sel_hi:[1,0]
	v_pk_add_f32 v[12:13], v[4:5], 1.0 op_sel_hi:[1,0]
	global_load_dwordx4 v[4:7], v[28:29], off offset:3072
	s_waitcnt vmcnt(0)
	v_pk_fma_f32 v[0:1], v[0:1], v[12:13], v[4:5]
	v_pk_fma_f32 v[6:7], v[8:9], v[10:11], v[6:7]
	v_cvt_pk_bf16_f32 v0, v0, v1
	s_nop 0
	v_cvt_pk_bf16_f32 v1, v6, v7
	global_store_dwordx2 v[2:3], v[0:1], off offset:3584
	s_branch .LBB0_1653
